# speedup vs baseline: 1.0166x; 1.0066x over previous
.LBB2_48:
	v_readlane_b32 s2, v35, 0
	v_readlane_b32 s3, v35, 16
	s_max_i32 s2, s2, s3
	v_readlane_b32 s3, v35, 32
	v_readlane_b32 s4, v35, 48
	s_nop 0
	v_mov_b32_e32 v2, s3
	v_mov_b32_e32 v3, s4
	v_max3_i32 v2, s2, v2, v3
	s_mov_b32 s2, 3
	v_readfirstlane_b32 s3, v2
	s_add_i32 s3, s3, 3
	s_mul_hi_i32 s3, s3, 0x55555556
	s_lshr_b32 s4, s3, 31
	s_add_i32 s3, s3, s4
	s_mul_i32 s3, s3, 3
	s_setprio 3
	s_cmp_gt_i32 s3, 30
	s_cbranch_scc1 .Ll1g_prc
	s_setprio 2
.Ll1g_prc:
	s_mov_b32 s21, s44
	s_cmp_eq_u32 s38, 1
	s_cbranch_scc1 .Ll1g_pre2
	ds_read_b96 v[62:64], v70 offset:768
	s_cmp_gt_i32 s3, 3
	s_cselect_b32 s4, 12, 0
	v_add_u32_e32 v73, s4, v70
	ds_read2_b32 v[66:67], v73 offset0:192 offset1:193
	ds_read_b32 v65, v73 offset:776
	s_waitcnt lgkmcnt(2)
	v_lshl_or_b32 v74, v62, 8, v71
	v_lshl_or_b32 v78, v63, 8, v71
	v_lshl_or_b32 v82, v64, 8, v71
	buffer_load_dwordx4 v[74:77], v74, s[20:23], 0 offen
	buffer_load_dwordx4 v[78:81], v78, s[20:23], 0 offen
	buffer_load_dwordx4 v[82:85], v82, s[20:23], 0 offen
	s_waitcnt lgkmcnt(0)
	v_lshl_or_b32 v86, v66, 8, v71
	v_lshl_or_b32 v90, v67, 8, v71
	v_lshl_or_b32 v50, v65, 8, v71
	buffer_load_dwordx4 v[86:89], v86, s[20:23], 0 offen
	buffer_load_dwordx4 v[90:93], v90, s[20:23], 0 offen
	buffer_load_dwordx4 v[50:53], v50, s[20:23], 0 offen

.LBB2_57:
	s_endpgm
	s_nop 0
	s_nop 0
	s_nop 0
	s_nop 0
	s_nop 0
	s_nop 0
	s_nop 0
	s_nop 0
	s_nop 0
	s_nop 0
	s_nop 0
	s_nop 0
	s_nop 0
	s_nop 0
	s_nop 0
	s_nop 0
	s_nop 0
	s_nop 0
	s_nop 0
	s_nop 0
	s_nop 0
	s_nop 0
	s_nop 0
	s_nop 0
	s_nop 0
	s_nop 0
	s_nop 0
	s_nop 0
	s_nop 0
	s_nop 0
	s_nop 0
	s_nop 0
	s_nop 0
	s_nop 0
	s_nop 0
	s_nop 0
	s_nop 0
	s_nop 0
	s_nop 0
	s_nop 0
	s_nop 0
	s_nop 0
	s_nop 0
	s_nop 0
	s_nop 0
	s_nop 0
	s_nop 0
	s_nop 0
	s_nop 0
	s_nop 0
	s_nop 0
	s_nop 0
	s_nop 0
	s_nop 0
	s_nop 0
	s_nop 0
	s_nop 0
	s_nop 0
	s_nop 0
	s_nop 0
	s_endpgm

.LBB3_32:
	s_or_b64 exec, exec, s[6:7]
	v_add_f32_e32 v17, 0, v17
	v_add_f32_e32 v13, v17, v13
	v_add_f32_e32 v9, v13, v9
	v_cvt_f32_i32_e32 v17, v37
	v_max_f32_e32 v22, v11, v11
	v_add_f32_dpp v9, v9, v9 quad_perm:[1,0,3,2] row_mask:0xf bank_mask:0xf
	v_max_f32_e32 v22, 0xff800000, v22
	v_max3_f32 v22, v22, v7, v14
	v_add_f32_dpp v9, v9, v9 quad_perm:[2,3,0,1] row_mask:0xf bank_mask:0xf
	s_nop 1
	v_add_f32_dpp v9, v9, v9 row_half_mirror row_mask:0xf bank_mask:0xf
	v_mov_b32_e32 v13, v9
	s_nop 1
	v_mov_b32_dpp v13, v13 row_mirror row_mask:0xf bank_mask:0xf
	s_waitcnt vmcnt(0)
	v_pk_add_f32 v[8:9], v[8:9], v[12:13]
	v_max_f32_e32 v12, 1.0, v17
	v_div_scale_f32 v13, s[6:7], v12, v12, v9
	v_rcp_f32_e32 v17, v13
	s_movk_i32 s7, 0x180
	s_mov_b32 s6, 0
	v_fma_f32 v23, -v13, v17, 1.0
	v_fmac_f32_e32 v17, v23, v17
	v_div_scale_f32 v23, vcc, v9, v12, v9
	v_mul_f32_e32 v24, v23, v17
	v_fma_f32 v25, -v13, v24, v23
	v_fmac_f32_e32 v24, v25, v17
	v_fma_f32 v13, -v13, v24, v23
	v_div_fmas_f32 v13, v13, v17, v24
	v_div_fixup_f32 v9, v13, v12, v9
	v_add_f32_e32 v8, v8, v9
	v_mul_f32_e32 v9, 0x3e4ccccd, v8
	v_cmp_lt_f32_e32 vcc, 0, v8
	s_nop 1
	v_cndmask_b32_e32 v8, v9, v8, vcc
	v_cmp_eq_u32_e32 vcc, v33, v37
	s_nop 0
	v_max_f32_dpp v9, v22, v22 quad_perm:[1,0,3,2] row_mask:0xf bank_mask:0xf
	s_nop 1
	v_max_f32_dpp v9, v9, v9 quad_perm:[2,3,0,1] row_mask:0xf bank_mask:0xf
	s_nop 1
	v_max_f32_dpp v9, v9, v9 row_half_mirror row_mask:0xf bank_mask:0xf
	s_nop 1
	v_max_f32_dpp v12, v9, v9 row_mirror row_mask:0xf bank_mask:0xf
	v_max_f32_e32 v9, v12, v8
	v_sub_f32_e32 v11, v11, v9
	v_mul_f32_e32 v11, 0x3fb8aa3b, v11
	v_sub_f32_e32 v7, v7, v9
	v_exp_f32_e32 v11, v11
	v_mul_f32_e32 v7, 0x3fb8aa3b, v7
	v_sub_f32_e32 v13, v14, v9
	v_exp_f32_e32 v7, v7
	v_mul_f32_e32 v13, 0x3fb8aa3b, v13
	v_exp_f32_e32 v13, v13
	v_add_f32_e32 v12, 0, v11
	v_cndmask_b32_e64 v12, 0, v12, s[0:1]
	v_cndmask_b32_e64 v14, 0, v7, s[2:3]
	v_add_f32_e32 v12, v12, v14
	v_cndmask_b32_e64 v14, 0, v13, s[4:5]
	v_add_f32_e32 v12, v12, v14
	v_sub_f32_e32 v8, v8, v9
	v_mul_f32_e32 v8, 0x3fb8aa3b, v8
	v_exp_f32_e32 v8, v8
	v_add_f32_dpp v9, v12, v12 quad_perm:[1,0,3,2] row_mask:0xf bank_mask:0xf
	s_nop 1
	v_add_f32_dpp v9, v9, v9 quad_perm:[2,3,0,1] row_mask:0xf bank_mask:0xf
	s_nop 1
	v_add_f32_dpp v9, v9, v9 row_half_mirror row_mask:0xf bank_mask:0xf
	s_nop 1
	v_add_f32_dpp v9, v9, v9 row_mirror row_mask:0xf bank_mask:0xf
	v_add_f32_e32 v9, v8, v9
	v_add_f32_e32 v9, 0x24e69595, v9
	v_rcp_f32_e32 v12, v9
	v_or_b32_e32 v9, s22, v36
	v_mul_lo_u32 v9, v9, s7
	v_or_b32_e32 v17, v9, v38
	v_mul_f32_e32 v22, v8, v12
	v_mul_f32_e32 v8, v12, v11
	v_cndmask_b32_e32 v9, 0, v22, vcc
	v_cmp_eq_u32_e32 vcc, v16, v37
	v_cndmask_b32_e64 v14, v9, v8, s[0:1]
	v_mul_f32_e32 v7, v12, v7
	v_cndmask_b32_e32 v8, 0, v22, vcc
	v_cndmask_b32_e64 v8, v8, v7, s[2:3]
	v_mov_b32_e32 v9, v10
	v_cmp_eq_u32_e32 vcc, v21, v37
	ds_write2_b64 v17, v[14:15], v[8:9] offset1:16
	v_mul_f32_e32 v7, v12, v13
	v_cndmask_b32_e32 v8, 0, v22, vcc
	v_readlane_b32 s0, v37, 0
	v_cndmask_b32_e64 v8, v8, v7, s[4:5]
	v_mov_b32_e32 v9, v6
	s_mul_i32 s7, s22, 0x180
	s_add_i32 s2, s0, 1
	ds_write_b64 v17, v[8:9] offset:256
	s_setprio 3
	v_readlane_b32 s1, v37, 16
	v_readlane_b32 s2, v37, 32
	v_readlane_b32 s3, v37, 48
	v_or_b32_e32 v6, s22, v36
	v_mul_u32_u24_e32 v6, 0x180, v6
	v_mov_b32_e32 v48, 0
	v_mov_b32_e32 v49, 0
	s_max_i32 s0, s0, s1
	s_max_i32 s2, s2, s3
	s_max_i32 s0, s0, s2
	s_add_i32 s0, s0, 4
	s_and_b32 s0, s0, -4
	s_cmp_gt_i32 s0, 28
	s_cbranch_scc1 .Ll2g_prc
	s_setprio 2
.Ll2g_prc:
	s_mov_b32 s1, 0
	v_mov_b32_e32 v50, 0
	v_mov_b32_e32 v51, 0
	ds_read2_b64 v[8:11], v6 offset0:0 offset1:1
	ds_read2_b64 v[12:15], v6 offset0:2 offset1:3
	s_waitcnt lgkmcnt(0)
	v_lshl_or_b32 v9, v9, 7, v38
	v_lshl_or_b32 v11, v11, 7, v38
	v_lshl_or_b32 v13, v13, 7, v38
	v_lshl_or_b32 v15, v15, 7, v38
	buffer_load_dwordx2 v[20:21], v9, s[12:15], 0 offen
	buffer_load_dwordx2 v[22:23], v11, s[12:15], 0 offen
	buffer_load_dwordx2 v[24:25], v13, s[12:15], 0 offen
	buffer_load_dwordx2 v[26:27], v15, s[12:15], 0 offen

.LBB3_55:
	s_waitcnt vmcnt(1)
	v_add_f32_e32 v7, v8, v14
	v_add_f32_e32 v7, v13, v7
	v_mul_f32_e32 v14, 0x3e4ccccd, v7
	v_cmp_lt_f32_e32 vcc, 0, v7
	s_nop 1
	v_cndmask_b32_e32 v7, v14, v7, vcc
	s_or_b64 exec, exec, s[6:7]
	v_mov_b32_e32 v14, 0xff800000
	s_and_saveexec_b64 s[6:7], s[4:5]
	s_cbranch_execnz .LBB3_31
	s_branch .LBB3_32
	s_nop 0
	s_nop 0
	s_nop 0
	s_nop 0
	s_nop 0
	s_nop 0
	s_nop 0
	s_nop 0
	s_nop 0
	s_nop 0
	s_nop 0
	s_nop 0
	s_endpgm
